# warmkd
# speedup vs baseline: 1.0206x; 1.0082x over previous
_Z11prep_kernelPKfS0_PKiS2_S0_S0_S0_S0_S0_S0_Pc:
	s_getpc_b64 s[36:37]
	s_add_u32 s36, s36, _Z11attn_kernelILi4EEvPKfS1_S1_S1_S1_S1_PKcPf@rel32@lo+4
	s_addc_u32 s37, s37, _Z11attn_kernelILi4EEvPKfS1_S1_S1_S1_S1_PKcPf@rel32@hi+12
	v_and_b32_e32 v192, 63, v0
	v_lshlrev_b32_e32 v192, 7, v192
	v_min_u32_e32 v192, 0x1180, v192
	global_load_dword v192, v192, s[36:37]
	s_getpc_b64 s[38:39]
	s_add_u32 s38, s38, _Z11attn_kernelILi4EEvPKfS1_S1_S1_S1_S1_PKcPf.kd@rel32@lo+4
	s_addc_u32 s39, s39, _Z11attn_kernelILi4EEvPKfS1_S1_S1_S1_S1_PKcPf.kd@rel32@hi+12
	v_mov_b32_e32 v193, 0
	global_load_dword v193, v193, s[38:39]
	s_lshr_b32 s4, s2, 2
	v_lshrrev_b32_e32 v2, 6, v0
	s_and_b32 s4, s4, 0x1ffffffe
	s_load_dwordx4 s[28:31], s[0:1], 0x40
	s_load_dwordx8 s[12:19], s[0:1], 0x0
	s_load_dwordx8 s[20:27], s[0:1], 0x20
	s_load_dwordx2 s[32:33], s[0:1], 0x50
	v_and_b32_e32 v1, 15, v0
	s_and_b32 s3, s2, 7
	v_or_b32_e32 v2, s4, v2
	v_lshl_or_b32 v88, v2, 3, s3
	v_cmp_gt_u32_e64 s[10:11], 14, v1
	v_mul_lo_u32 v7, v88, 14
	v_and_b32_e32 v105, 63, v0
	v_cndmask_b32_e64 v6, 13, v1, s[10:11]
	v_add_u32_e32 v2, v7, v6
	v_mul_u32_u24_e32 v4, 12, v2
	v_lshlrev_b32_e32 v5, 2, v6
	v_cmp_gt_u32_e64 s[8:9], 48, v105
	v_cmp_gt_u32_e64 s[6:7], 14, v105
	v_lshlrev_b32_e32 v118, 1, v0
	v_lshrrev_b32_e32 v104, 4, v0
	v_cndmask_b32_e64 v8, 0, v105, s[8:9]
	v_cndmask_b32_e64 v9, 0, v105, s[6:7]
	v_mad_u32_u24 v8, v88, 48, v8
	v_add_lshl_u32 v9, v7, v9, 2
	v_lshlrev_b32_e32 v8, 2, v8
	s_lshl_b32 s2, s2, 3
	s_and_b32 s2, s2, 0x78
	v_and_b32_e32 v106, 30, v118
	v_or_b32_e32 v107, s2, v104
	v_cmp_gt_u32_e64 s[2:3], 23, v106
	v_or_b32_e32 v10, 1, v106
	v_cmp_gt_u32_e64 s[4:5], 23, v10
	v_lshlrev_b32_e32 v11, 7, v106
	v_lshlrev_b32_e32 v10, 7, v10
	v_cndmask_b32_e64 v11, 0, v11, s[2:3]
	v_cndmask_b32_e64 v10, 0, v10, s[4:5]
	v_or_b32_e32 v11, v11, v107
	v_or_b32_e32 v10, v10, v107
	v_lshlrev_b32_e32 v11, 2, v11
	v_lshlrev_b32_e32 v10, 2, v10
	v_lshlrev_b32_e32 v12, 2, v107
	v_lshlrev_b32_e32 v119, 5, v0
	v_lshlrev_b32_e32 v13, 2, v0
	v_and_b32_e32 v109, 12, v13
	v_and_b32_e32 v91, 0xf80, v119
	v_lshl_or_b32 v91, v109, 2, v91
	v_or_b32_e32 v92, 0x1000, v91
	v_lshlrev_b32_e32 v90, 9, v2
	v_and_b32_e32 v16, 48, v0
	v_or_b32_e32 v90, v90, v16
	v_or_b32_e32 v112, 0x80, v0
	v_or_b32_e32 v111, 0x180, v0
	v_or_b32_e32 v108, 0x280, v0
	v_mov_b32_e32 v87, 0
	v_bfe_u32 v110, v0, 4, 2
	s_movk_i32 s34, 0x60
	v_lshrrev_b32_e32 v136, 1, v0
	v_lshrrev_b32_e32 v18, 3, v0
	v_and_b32_e32 v18, 4, v18
	v_and_b32_e32 v19, 24, v0
	v_and_b32_e32 v20, 2, v136
	v_or3_b32 v18, v18, v19, v20
	v_and_or_b32 v136, v136, s34, v18
	v_mul_u32_u24_e32 v18, 0x110, v109
	v_lshl_add_u32 v136, v136, 1, v18
	v_add_u32_e32 v137, 0x1100, v136
	v_add_u32_e32 v138, 0x2200, v136
	v_lshlrev_b32_e32 v18, 9, v88
	v_and_b32_e32 v19, 0x100, v119
	v_lshlrev_b32_e32 v20, 4, v0
	v_and_b32_e32 v20, 48, v20
	v_or3_b32 v139, v18, v19, v20
	v_and_b32_e32 v19, 8, v118
	v_and_b32_e32 v20, 64, v118
	v_or3_b32 v139, v139, v19, v20
	v_lshlrev_b32_e32 v19, 2, v110
	v_and_b32_e32 v20, 4, v19
	v_or_b32_e32 v139, v139, v20
	v_lshl_or_b32 v140, v1, 5, v18
	v_or_b32_e32 v140, v140, v19
	v_add_u32_e32 v140, 0x80000, v140
	v_lshl_or_b32 v141, v88, 4, v1
	v_lshlrev_b32_e32 v141, 3, v141
	v_add_u32_e32 v141, 0x140000, v141
	v_lshlrev_b32_e32 v20, 8, v88
	v_mul_u32_u24_e32 v21, 43, v105
	v_lshrrev_b32_e32 v21, 9, v21
	v_mul_u32_u24_e32 v21, 12, v21
	v_sub_u32_e32 v22, v105, v21
	v_and_b32_e32 v142, 3, v22
	v_lshrrev_b32_e32 v22, 2, v22
	v_mad_u32_u24 v142, v142, 3, v22
	v_add_u32_e32 v142, v142, v21
	v_lshl_add_u32 v142, v142, 2, v20
	v_add_u32_e32 v142, 0x164000, v142
	v_lshl_add_u32 v143, v105, 2, v20
	v_add_u32_e32 v143, 0x164000, v143
	v_lshlrev_b32_e32 v123, 6, v107
	v_lshl_add_u32 v123, v106, 1, v123
	v_add_u32_e32 v123, 0x160000, v123
	v_lshl_add_u32 v122, v1, 4, v20
	v_or_b32_e32 v122, v122, v19
	v_add_u32_e32 v122, 0x100000, v122
	s_waitcnt lgkmcnt(0)
	global_load_dwordx3 v[82:84], v4, s[12:13]
	global_load_dword v85, v5, s[26:27]
	global_load_dword v114, v8, s[18:19]
	global_load_dword v115, v9, s[16:17]
	global_load_dword v116, v11, s[28:29]
	global_load_dword v113, v10, s[28:29]
	global_load_dword v117, v12, s[30:31]
	global_load_dwordx4 v[66:69], v91, s[20:21]
	global_load_dwordx4 v[70:73], v91, s[20:21] offset:64
	global_load_dwordx4 v[74:77], v92, s[20:21]
	global_load_dwordx4 v[78:81], v92, s[20:21] offset:64
	global_load_dwordx4 v[58:61], v91, s[22:23]
	global_load_dwordx4 v[62:65], v91, s[22:23] offset:64
	global_load_dwordx4 v[50:53], v92, s[22:23]
	global_load_dwordx4 v[54:57], v92, s[22:23] offset:64
	global_load_dwordx4 v[42:45], v91, s[24:25]
	global_load_dwordx4 v[46:49], v91, s[24:25] offset:64
	global_load_dwordx4 v[34:37], v92, s[24:25]
	global_load_dwordx4 v[38:41], v92, s[24:25] offset:64
	global_load_dwordx4 v[26:29], v90, s[14:15] nt
	global_load_dwordx4 v[30:33], v90, s[14:15] offset:64 nt
	global_load_dwordx4 v[18:21], v90, s[14:15] offset:128 nt
	global_load_dwordx4 v[22:25], v90, s[14:15] offset:192 nt
	global_load_dwordx4 v[10:13], v90, s[14:15] offset:256 nt
	global_load_dwordx4 v[14:17], v90, s[14:15] offset:320 nt
	global_load_dwordx4 v[2:5], v90, s[14:15] offset:384 nt
	global_load_dwordx4 v[6:9], v90, s[14:15] offset:448 nt
	s_waitcnt vmcnt(26)
	v_mov_b32_e32 v90, v83
	v_mov_b32_e32 v91, v84
	v_lshlrev_b32_e32 v86, 2, v110
	s_waitcnt vmcnt(25)
	v_mul_f32_e32 v84, 0x3fb8aa3b, v85
	s_mov_b32 s14, 0x41700000
	v_exp_f32_e32 v84, v84
	v_cndmask_b32_e64 v94, 0, 1.0, s[10:11]
	v_add_f32_e32 v84, 1.0, v84
	v_cmp_lt_f32_e32 vcc, s14, v85
	v_log_f32_e32 v84, v84
	v_cmp_lt_u32_e64 s[12:13], 15, v105
	v_mul_f32_e32 v84, 0x3f317218, v84
	v_cndmask_b32_e32 v84, v84, v85, vcc
	v_mul_f32_e32 v84, 0xbe715bef, v84
	v_mul_f32_e32 v84, 0x3f3504f3, v84
	v_mul_f32_e32 v84, 0x41800000, v84
	v_cndmask_b32_e64 v99, 0, v84, s[10:11]
	v_mul_f32_e32 v101, -2.0, v99
	v_mul_f32_e32 v100, v82, v82
	v_cmp_gt_u32_e32 vcc, 16, v105
	v_fmac_f32_e32 v100, v90, v90
	v_cmp_eq_u32_e64 s[12:13], 0, v110
	v_fmac_f32_e32 v100, v91, v91
	v_cmp_eq_u32_e64 s[14:15], 1, v110
	v_mul_f32_e32 v83, v101, v82
	v_cmp_eq_u32_e64 s[16:17], 2, v110
	v_mul_f32_e32 v84, v101, v90
	v_mul_f32_e32 v85, v101, v91
	v_mul_f32_e32 v89, v99, v100
	v_mul_f32_e32 v92, v82, v94
	v_mul_f32_e32 v93, v90, v94
	v_mul_f32_e32 v95, v91, v94
	v_mul_f32_e32 v96, v100, v94
	v_cvt_pk_fp8_f32 v88, v83, v83
	v_cvt_pk_fp8_f32 v104, v84, v84
	v_cvt_f32_fp8_e32 v97, v88
	v_cvt_f32_fp8_e32 v98, v104
	v_sub_f32_e32 v97, v83, v97
	v_sub_f32_e32 v98, v84, v98
	v_cvt_pk_fp8_f32 v88, v85, v85
	v_cvt_pk_fp8_f32 v104, v99, v99
	v_cvt_f32_fp8_e32 v101, v88
	v_cvt_f32_fp8_e32 v102, v104
	v_sub_f32_e32 v101, v85, v101
	v_sub_f32_e32 v102, v99, v102
	v_cvt_pk_fp8_f32 v88, v89, v89
	v_cvt_pk_fp8_f32 v104, v92, v92
	v_cvt_f32_fp8_e32 v103, v88
	v_cvt_f32_fp8_e32 v120, v104
	v_sub_f32_e32 v103, v89, v103
	v_sub_f32_e32 v120, v92, v120
	v_cvt_pk_fp8_f32 v88, v93, v93
	v_cvt_pk_fp8_f32 v104, v95, v95
	v_cvt_f32_fp8_e32 v121, v88
	v_cvt_f32_fp8_e32 v86, v104
	v_sub_f32_e32 v121, v93, v121
	v_sub_f32_e32 v86, v95, v86
	v_cvt_pk_fp8_f32 v88, v96, v96
	s_nop 0
	v_cvt_f32_fp8_e32 v87, v88
	s_nop 0
	v_sub_f32_e32 v87, v96, v87
	v_cndmask_b32_e64 v124, v89, v85, s[16:17]
	v_cndmask_b32_e64 v124, v124, v98, s[14:15]
	v_cndmask_b32_e64 v124, v124, v83, s[12:13]
	v_cndmask_b32_e64 v125, v103, v99, s[16:17]
	v_cndmask_b32_e64 v125, v125, v84, s[14:15]
	v_cndmask_b32_e64 v125, v125, v97, s[12:13]
	v_cndmask_b32_e64 v126, 0, v102, s[16:17]
	v_cndmask_b32_e64 v126, v126, v85, s[14:15]
	v_cndmask_b32_e64 v126, v126, v83, s[12:13]
	v_cndmask_b32_e64 v127, 0, v99, s[16:17]
	v_cndmask_b32_e64 v127, v127, v101, s[14:15]
	v_cndmask_b32_e64 v127, v127, v84, s[12:13]
	v_cndmask_b32_e64 v128, v94, v86, s[16:17]
	v_cndmask_b32_e64 v128, v128, v93, s[14:15]
	v_cndmask_b32_e64 v128, v128, v92, s[12:13]
	v_cndmask_b32_e64 v129, v94, v96, s[16:17]
	v_cndmask_b32_e64 v129, v129, v121, s[14:15]
	v_cndmask_b32_e64 v129, v129, v92, s[12:13]
	v_cndmask_b32_e64 v130, 0, v96, s[16:17]
	v_cndmask_b32_e64 v130, v130, v95, s[14:15]
	v_cndmask_b32_e64 v130, v130, v120, s[12:13]
	v_cndmask_b32_e64 v131, 0, v87, s[16:17]
	v_cndmask_b32_e64 v131, v131, v95, s[14:15]
	v_cndmask_b32_e64 v131, v131, v93, s[12:13]
	v_cvt_pk_fp8_f32 v119, v124, v125
	v_cvt_pk_fp8_f32 v103, v128, v129
	v_cvt_pk_fp8_f32 v119, v126, v127 op_sel:[0,0,1]
	v_cvt_pk_fp8_f32 v103, v130, v131 op_sel:[0,0,1]
	s_nop 0
	global_store_dword v139, v119, s[32:33] offset:128
	global_store_dword v140, v103, s[32:33] offset:16
	s_and_saveexec_b64 s[0:1], vcc
	s_cbranch_execz .LBB0_14
	v_cvt_f16_f32_e32 v83, v82
	v_cvt_pk_f16_f32 v90, v90, v91
	s_nop 0
	v_alignbit_b32 v91, 0, v90, 16
	v_pack_b32_f16 v90, v83, v90
	global_store_dwordx2 v141, v[90:91], s[32:33]
